# tile decode in the fp8 GEMM headers: quotient and remainder by the group size take a shift and mask path when the group has all 8 row tiles (generic reciprocal division kept for the last group)
# baseline (speedup 1.0000x reference)
.LBB0_543:
	s_add_i32 s58, s58, 1
	s_mul_i32 s1, s58, s57
	s_mul_hi_u32 s2, s58, s29
	s_add_i32 s2, s2, s1
	s_mul_i32 s1, s58, s29
	s_add_u32 s16, s1, s28
	s_addc_u32 s17, s2, s36
	v_mov_b64_e32 v[2:3], 0x600
	v_cmp_lt_i64_e64 s[2:3], s[16:17], v[2:3]
	v_mov_b64_e32 v[2:3], 0x5ff
	v_cmp_gt_i64_e32 vcc, s[16:17], v[2:3]
	v_mov_b32_e32 v184, 1
	s_cbranch_vccnz .LBB0_545
	s_ashr_i32 s1, s16, 31
	s_lshr_b32 s1, s1, 29
	s_add_i32 s1, s16, s1
	s_ashr_i32 s12, s1, 3
	s_and_b32 s1, s1, -8
	s_sub_i32 s1, s16, s1
	s_cmp_lt_i32 s1, 0
	s_movk_i32 s13, 0xc1
	s_cselect_b32 s13, s13, 0xc0
	s_mul_i32 s1, s13, s1
	s_add_i32 s1, s1, s12
	s_mul_hi_i32 s12, s1, 0x2aaaaaab
	s_lshr_b32 s13, s12, 31
	s_ashr_i32 s12, s12, 4
	s_add_i32 s12, s12, s13
	s_lshl_b32 s13, s12, 3
	s_sub_i32 s14, 0x80, s13
	s_min_i32 s14, s14, 8
	s_mulk_i32 s12, 0x60
	s_sub_i32 s1, s1, s12
	s_cmp_eq_u32 s14, 8
	s_cbranch_scc1 .Lfd_2
	s_abs_i32 s15, s14
	v_cvt_f32_u32_e32 v0, s15
	s_sub_i32 s17, 0, s15
	v_rcp_iflag_f32_e32 v0, v0
	s_abs_i32 s12, s1
	s_xor_b32 s16, s1, s14
	s_ashr_i32 s16, s16, 31
	v_mul_f32_e32 v0, 0x4f7ffffe, v0
	v_cvt_u32_f32_e32 v0, v0
	s_nop 0
	v_readfirstlane_b32 s18, v0
	s_mul_i32 s17, s17, s18
	s_mul_hi_u32 s17, s18, s17
	s_add_i32 s18, s18, s17
	s_mul_hi_u32 s17, s12, s18
	s_mul_i32 s18, s17, s15
	s_sub_i32 s12, s12, s18
	s_add_i32 s19, s17, 1
	s_sub_i32 s18, s12, s15
	s_cmp_ge_u32 s12, s15
	s_cselect_b32 s17, s19, s17
	s_cselect_b32 s12, s18, s12
	s_add_i32 s18, s17, 1
	s_cmp_ge_u32 s12, s15
	s_cselect_b32 s12, s18, s17
	s_xor_b32 s12, s12, s16
	s_sub_i32 s12, s12, s16
	s_mul_i32 s14, s12, s14
	s_sub_i32 s1, s1, s14
	s_branch .Lfj_2
.Lfd_2:
	s_lshr_b32 s12, s1, 3
	s_and_b32 s1, s1, 7
.Lfj_2:
	s_add_i32 s14, s1, s13

.LBB0_576:
	s_ashr_i32 s10, s12, 3
	s_add_i32 s10, s14, s10
	s_ashr_i32 s11, s10, 31
	s_lshr_b32 s11, s11, 22
	s_add_i32 s11, s10, s11
	s_ashr_i32 s12, s11, 10
	s_lshl_b32 s12, s12, 3
	s_sub_i32 s13, 8, s12
	s_min_i32 s13, s13, 8
	s_and_b32 s11, s11, 0xfffffc00
	s_sub_i32 s11, s10, s11
	s_cmp_eq_u32 s13, 8
	s_cbranch_scc1 .Lfd_3
	s_abs_i32 s14, s13
	v_cvt_f32_u32_e32 v0, s14
	s_sub_i32 s18, 0, s14
	v_rcp_iflag_f32_e32 v0, v0
	s_abs_i32 s10, s11
	s_xor_b32 s15, s11, s13
	s_ashr_i32 s15, s15, 31
	v_mul_f32_e32 v0, 0x4f7ffffe, v0
	v_cvt_u32_f32_e32 v0, v0
	s_nop 0
	v_readfirstlane_b32 s19, v0
	s_mul_i32 s18, s18, s19
	s_mul_hi_u32 s18, s19, s18
	s_add_i32 s19, s19, s18
	s_mul_hi_u32 s18, s10, s19
	s_mul_i32 s19, s18, s14
	s_sub_i32 s10, s10, s19
	s_add_i32 s24, s18, 1
	s_sub_i32 s19, s10, s14
	s_cmp_ge_u32 s10, s14
	s_cselect_b32 s18, s24, s18
	s_cselect_b32 s10, s19, s10
	s_add_i32 s19, s18, 1
	s_cmp_ge_u32 s10, s14
	s_cselect_b32 s10, s19, s18
	s_xor_b32 s10, s10, s15
	s_sub_i32 s10, s10, s15
	s_mul_i32 s13, s10, s13
	s_sub_i32 s11, s11, s13
	s_branch .Lfj_3
.Lfd_3:
	s_lshr_b32 s10, s11, 3
	s_and_b32 s11, s11, 7
.Lfj_3:
	s_add_i32 s12, s12, s11

.LBB0_592:
	s_add_i32 s58, s58, 1
	s_mul_i32 s1, s58, s57
	s_mul_hi_u32 s2, s58, s29
	s_add_i32 s2, s2, s1
	s_mul_i32 s1, s58, s29
	s_add_u32 s16, s1, s28
	s_addc_u32 s17, s2, s36
	v_mov_b64_e32 v[2:3], 0x600
	v_cmp_lt_i64_e64 s[2:3], s[16:17], v[2:3]
	v_mov_b64_e32 v[2:3], 0x5ff
	v_cmp_gt_i64_e32 vcc, s[16:17], v[2:3]
	v_mov_b32_e32 v243, 1
	s_cbranch_vccnz .LBB0_594
	s_ashr_i32 s1, s16, 31
	s_lshr_b32 s1, s1, 29
	s_add_i32 s1, s16, s1
	s_ashr_i32 s12, s1, 3
	s_and_b32 s1, s1, -8
	s_sub_i32 s1, s16, s1
	s_cmp_lt_i32 s1, 0
	s_movk_i32 s13, 0xc1
	s_cselect_b32 s13, s13, 0xc0
	s_mul_i32 s1, s13, s1
	s_add_i32 s1, s1, s12
	s_mul_hi_i32 s12, s1, 0x2aaaaaab
	s_lshr_b32 s13, s12, 31
	s_ashr_i32 s12, s12, 4
	s_add_i32 s12, s12, s13
	s_lshl_b32 s13, s12, 3
	s_sub_i32 s14, 0x80, s13
	s_min_i32 s14, s14, 8
	s_mulk_i32 s12, 0x60
	s_sub_i32 s1, s1, s12
	s_cmp_eq_u32 s14, 8
	s_cbranch_scc1 .Lfd_4
	s_abs_i32 s15, s14
	v_cvt_f32_u32_e32 v0, s15
	s_sub_i32 s17, 0, s15
	v_rcp_iflag_f32_e32 v0, v0
	s_abs_i32 s12, s1
	s_xor_b32 s16, s1, s14
	s_ashr_i32 s16, s16, 31
	v_mul_f32_e32 v0, 0x4f7ffffe, v0
	v_cvt_u32_f32_e32 v0, v0
	s_nop 0
	v_readfirstlane_b32 s18, v0
	s_mul_i32 s17, s17, s18
	s_mul_hi_u32 s17, s18, s17
	s_add_i32 s18, s18, s17
	s_mul_hi_u32 s17, s12, s18
	s_mul_i32 s18, s17, s15
	s_sub_i32 s12, s12, s18
	s_add_i32 s19, s17, 1
	s_sub_i32 s18, s12, s15
	s_cmp_ge_u32 s12, s15
	s_cselect_b32 s17, s19, s17
	s_cselect_b32 s12, s18, s12
	s_add_i32 s18, s17, 1
	s_cmp_ge_u32 s12, s15
	s_cselect_b32 s12, s18, s17
	s_xor_b32 s12, s12, s16
	s_sub_i32 s12, s12, s16
	s_mul_i32 s14, s12, s14
	s_sub_i32 s1, s1, s14
	s_branch .Lfj_4

.LBB0_1240:
	s_add_i32 s60, s63, 1
	s_mul_i32 s2, s60, s0
	s_mul_hi_u32 s3, s60, s38
	s_add_i32 s3, s3, s2
	s_mul_i32 s2, s60, s38
	s_add_u32 s24, s2, s4
	s_addc_u32 s25, s3, s5
	v_mov_b64_e32 v[2:3], s[6:7]
	v_cmp_ge_i64_e32 vcc, s[24:25], v[2:3]
	v_mov_b32_e32 v243, 1
	v_cmp_lt_i64_e64 s[2:3], s[24:25], v[2:3]
	s_cbranch_vccnz .LBB0_1242
	s_ashr_i32 s20, s24, 31
	s_lshr_b32 s20, s20, 29
	s_add_i32 s20, s24, s20
	s_ashr_i32 s21, s20, 3
	s_and_b32 s20, s20, -8
	s_sub_i32 s20, s24, s20
	s_cmp_lt_i32 s20, 0
	s_cselect_b32 s22, s40, s39
	s_mul_i32 s20, s22, s20
	s_add_i32 s20, s20, s21
	s_ashr_i32 s21, s20, 31
	s_lshr_b32 s21, s21, 26
	s_add_i32 s21, s20, s21
	s_ashr_i32 s22, s21, 6
	s_lshl_b32 s22, s22, 3
	s_sub_i32 s23, s39, s22
	s_min_i32 s23, s23, 8
	s_andn2_b32 s21, s21, 63
	s_sub_i32 s21, s20, s21
	s_cmp_eq_u32 s23, 8
	s_cbranch_scc1 .Lfd_0
	s_abs_i32 s24, s23
	v_cvt_f32_u32_e32 v0, s24
	s_sub_i32 s30, 0, s24
	v_rcp_iflag_f32_e32 v0, v0
	s_abs_i32 s20, s21
	s_xor_b32 s25, s21, s23
	s_ashr_i32 s25, s25, 31
	v_mul_f32_e32 v0, 0x4f7ffffe, v0
	v_cvt_u32_f32_e32 v0, v0
	s_nop 0
	v_readfirstlane_b32 s31, v0
	s_mul_i32 s30, s30, s31
	s_mul_hi_u32 s30, s31, s30
	s_add_i32 s31, s31, s30
	s_mul_hi_u32 s30, s20, s31
	s_mul_i32 s31, s30, s24
	s_sub_i32 s20, s20, s31
	s_add_i32 s34, s30, 1
	s_sub_i32 s31, s20, s24
	s_cmp_ge_u32 s20, s24
	s_cselect_b32 s30, s34, s30
	s_cselect_b32 s20, s31, s20
	s_add_i32 s31, s30, 1
	s_cmp_ge_u32 s20, s24
	s_cselect_b32 s20, s31, s30
	s_xor_b32 s20, s20, s25
	s_sub_i32 s20, s20, s25
	s_mul_i32 s23, s20, s23
	s_sub_i32 s21, s21, s23
	s_branch .Lfj_0
.Lfd_0:
	s_lshr_b32 s20, s21, 3
	s_and_b32 s21, s21, 7
.Lfj_0:
	s_add_i32 s61, s21, s22
	s_lshl_b32 s21, s61, 2
	s_add_i32 s21, s15, s21
	v_mov_b32_e32 v0, s21
	ds_read_b32 v0, v0
	s_waitcnt lgkmcnt(0)
	v_readfirstlane_b32 s22, v0

.LBB0_1347:
	s_ashr_i32 s12, s14, 3
	s_add_i32 s12, s16, s12
	s_ashr_i32 s13, s12, 31
	s_lshr_b32 s13, s13, 27
	s_add_i32 s13, s12, s13
	s_ashr_i32 s14, s13, 5
	s_lshl_b32 s14, s14, 3
	s_sub_i32 s15, s34, s14
	s_min_i32 s15, s15, 8
	s_andn2_b32 s13, s13, 31
	s_sub_i32 s13, s12, s13
	s_cmp_eq_u32 s15, 8
	s_cbranch_scc1 .Lfd_1
	s_abs_i32 s16, s15
	v_cvt_f32_u32_e32 v0, s16
	s_sub_i32 s18, 0, s16
	v_rcp_iflag_f32_e32 v0, v0
	s_abs_i32 s12, s13
	s_xor_b32 s17, s13, s15
	s_ashr_i32 s17, s17, 31
	v_mul_f32_e32 v0, 0x4f7ffffe, v0
	v_cvt_u32_f32_e32 v0, v0
	s_nop 0
	v_readfirstlane_b32 s19, v0
	s_mul_i32 s18, s18, s19
	s_mul_hi_u32 s18, s19, s18
	s_add_i32 s19, s19, s18
	s_mul_hi_u32 s18, s12, s19
	s_mul_i32 s19, s18, s16
	s_sub_i32 s12, s12, s19
	s_add_i32 s20, s18, 1
	s_sub_i32 s19, s12, s16
	s_cmp_ge_u32 s12, s16
	s_cselect_b32 s18, s20, s18
	s_cselect_b32 s12, s19, s12
	s_add_i32 s19, s18, 1
	s_cmp_ge_u32 s12, s16
	s_cselect_b32 s12, s19, s18
	s_xor_b32 s12, s12, s17
	s_sub_i32 s12, s12, s17
	s_mul_i32 s15, s12, s15
	s_sub_i32 s13, s13, s15
	s_branch .Lfj_1
.Lfd_1:
	s_lshr_b32 s12, s13, 3
	s_and_b32 s13, s13, 7
.Lfj_1:
	s_add_i32 s14, s14, s13
	s_lshl_b32 s13, s14, 2
	s_add_i32 s13, s33, s13
	v_mov_b32_e32 v0, s13
	ds_read_b32 v0, v0
	s_waitcnt lgkmcnt(0)
	v_readfirstlane_b32 s16, v0
